# scatter: the two 16-way LDS partial-sum reductions issue all reads before one wait
# speedup vs baseline: 1.0021x; 1.0021x over previous
.LBB0_1843:
	s_or_b64 exec, exec, s[4:5]
	v_lshl_add_u32 v10, v2, 2, 0
	v_cmp_gt_i32_e64 s[0:1], 32, v2
	v_add_u32_e32 v11, 0x400, v10
	v_add_u32_e32 v12, 0x800, v10
	ds_write_b32 v10, v3 offset:384
	s_waitcnt lgkmcnt(0)
	s_barrier
	s_and_saveexec_b64 s[4:5], s[0:1]
	s_cbranch_execz .LBB0_1846
	ds_read2_b32 v[46:47], v10 offset0:96 offset1:128
	v_add_u32_e32 v5, 0x200, v10
	s_cmp_eq_u32 s25, 0
	ds_read2_b32 v[48:49], v10 offset0:160 offset1:192
	ds_read2_b32 v[50:51], v5 offset0:96 offset1:128
	v_add_u32_e32 v6, 0x600, v10
	ds_read2_b32 v[52:53], v11 offset0:32 offset1:64
	ds_read2_b32 v[54:55], v11 offset0:96 offset1:128
	ds_read2_b32 v[56:57], v11 offset0:160 offset1:192
	ds_read2_b32 v[58:59], v6 offset0:96 offset1:128
	ds_read2_b32 v[60:61], v12 offset0:32 offset1:64
	s_waitcnt lgkmcnt(0)
	v_add_u32_e32 v3, v47, v46
	v_add3_u32 v3, v3, v48, v49
	v_add3_u32 v3, v3, v50, v51
	v_add3_u32 v3, v3, v52, v53
	v_add3_u32 v3, v3, v54, v55
	v_add3_u32 v3, v3, v56, v57
	v_add3_u32 v3, v3, v58, v59
	v_add3_u32 v5, v3, v60, v61
	ds_write_b32 v10, v5 offset:2432
	s_cbranch_scc0 .LBB0_1846
	v_ashrrev_i32_e32 v3, 31, v2
	v_lshl_add_u64 v[6:7], v[2:3], 2, s[2:3]
	v_add_co_u32_e32 v6, vcc, 0x556ec000, v6
	s_nop 1
	v_addc_co_u32_e32 v7, vcc, 0, v7, vcc
	global_store_dword v[6:7], v5, off offset:2048

.LBB0_1873:
	s_or_b64 exec, exec, s[16:17]
	ds_write_b32 v10, v13 offset:384
	s_waitcnt lgkmcnt(0)
	s_barrier
	s_and_saveexec_b64 s[2:3], s[0:1]
	s_cbranch_execz .LBB0_1875
	ds_read2_b32 v[46:47], v10 offset0:32 offset1:96
	ds_read2_b32 v[48:49], v10 offset0:128 offset1:160
	ds_read2_b32 v[50:51], v10 offset0:192 offset1:224
	ds_read2_b32 v[52:53], v11 offset1:32
	ds_read2_b32 v[54:55], v11 offset0:64 offset1:96
	ds_read2_b32 v[56:57], v11 offset0:128 offset1:160
	ds_read2_b32 v[58:59], v11 offset0:192 offset1:224
	ds_read2_b32 v[60:61], v12 offset1:32
	ds_read_b32 v62, v10 offset:2304
	s_waitcnt vmcnt(8)
	s_waitcnt lgkmcnt(0)
	v_add3_u32 v6, v47, v46, v48
	v_add3_u32 v6, v6, v49, v50
	v_add3_u32 v6, v6, v51, v52
	v_add3_u32 v6, v6, v53, v54
	v_add3_u32 v6, v6, v55, v56
	v_add3_u32 v6, v6, v57, v58
	v_add3_u32 v6, v6, v59, v60
	v_add3_u32 v6, v6, v61, v62
	ds_write_b32 v10, v6 offset:2560
